# adds: U2 (fp8 MoE input) rows padded to 2176 B so gathered token rows spread over L2 channels
# speedup vs baseline: 1.0129x; 1.0022x over previous
; __device__ __forceinline__ float bf_lo(unsigned u) { return __uint_as_float(u << 16); }
; __device__ __forceinline__ float bf_hi(unsigned u) { return __uint_as_float(u & 0xffff0000u); }
; __device__ __forceinline__ void p6_router(Ctx& X) {
;     ...
;         { u32x2 hv[4][8];
; #pragma unroll
;           for (int r = 0; r < 4; ++r) { const u32x2* hr = (const u32x2*)(XP_Hh(X) + (size_t)(tb + 4 * w + r) * D) + lane;
; #pragma unroll
;               for (int j = 0; j < 8; ++j) hv[r][j] = hr[64 * j]; }
;           f32x4 wv[8]; { const f32x4* wr_ = (const f32x4*)XP_ln_ffn_w(X) + lane;
; #pragma unroll
;               for (int j = 0; j < 8; ++j) wv[j] = wr_[64 * j]; }
; #pragma unroll
;           for (int r = 0; r < 4; ++r) { const int tk = 4 * w + r, t = tb + tk; const float rstd = rs[tk];
;               unsigned* o8 = (unsigned*)(XP_U2(X) + (size_t)t * D) + lane;
; #pragma unroll
;               for (int j = 0; j < 8; ++j) { const u32x2 v = hv[r][j]; o8[64 * j] = pk_fp8x4(bf_lo(v.x) * rstd * wv[j].x, bf_hi(v.x) * rstd * wv[j].y, bf_lo(v.y) * rstd * wv[j].z, bf_hi(v.y) * rstd * wv[j].w); } } }
.LBB0_815:
	s_or_b64 exec, exec, s[44:45]
	s_add_i32 s8, s53, s33
	s_ashr_i32 s9, s8, 31
	s_lshl_b64 s[10:11], s[8:9], 12
	v_lshl_add_u64 v[60:61], v[42:43], 0, s[10:11]
	global_load_dwordx2 v[126:127], v[60:61], off
	global_load_dwordx2 v[128:129], v[60:61], off offset:512
	global_load_dwordx4 v[34:37], v[44:45], off
	global_load_dwordx4 v[30:33], v[44:45], off offset:1024
	global_load_dwordx4 v[26:29], v[44:45], off offset:2048
	global_load_dwordx4 v[22:25], v[44:45], off offset:3072
	global_load_dwordx4 v[18:21], v[46:47], off
	global_load_dwordx4 v[10:13], v[48:49], off
	global_load_dwordx4 v[6:9], v[50:51], off
	global_load_dwordx4 v[2:5], v[52:53], off
	global_load_dwordx2 v[130:131], v[60:61], off offset:1024
	v_mov_b32_e32 v14, s46
	ds_read_b128 v[14:17], v14 offset:37888
	global_load_dwordx2 v[134:135], v[60:61], off offset:1536
	global_load_dwordx2 v[136:137], v[60:61], off offset:2048
	global_load_dwordx2 v[138:139], v[60:61], off offset:2560
	global_load_dwordx2 v[140:141], v[60:61], off offset:3072
	global_load_dwordx2 v[142:143], v[60:61], off offset:3584
	s_or_b32 s10, s8, 1
	s_or_b32 s12, s8, 2
	s_or_b32 s14, s8, 3
	s_ashr_i32 s11, s10, 31
	s_ashr_i32 s13, s12, 31
	s_ashr_i32 s15, s14, 31
	s_lshl_b64 s[10:11], s[10:11], 12
	s_lshl_b64 s[12:13], s[12:13], 12
	s_lshl_b64 s[14:15], s[14:15], 12
	v_lshl_add_u64 v[60:61], v[42:43], 0, s[10:11]
	v_lshl_add_u64 v[62:63], v[42:43], 0, s[12:13]
	v_lshl_add_u64 v[144:145], v[42:43], 0, s[14:15]
	global_load_dwordx2 v[146:147], v[60:61], off
	global_load_dwordx2 v[148:149], v[60:61], off offset:512
	global_load_dwordx2 v[102:103], v[60:61], off offset:1024
	global_load_dwordx2 v[100:101], v[60:61], off offset:1536
	global_load_dwordx2 v[98:99], v[60:61], off offset:2048
	global_load_dwordx2 v[96:97], v[60:61], off offset:2560
	global_load_dwordx2 v[94:95], v[60:61], off offset:3072
	global_load_dwordx2 v[92:93], v[60:61], off offset:3584
	global_load_dwordx2 v[90:91], v[62:63], off
	global_load_dwordx2 v[88:89], v[62:63], off offset:512
	global_load_dwordx2 v[86:87], v[62:63], off offset:1024
	global_load_dwordx2 v[84:85], v[62:63], off offset:1536
	global_load_dwordx2 v[82:83], v[62:63], off offset:2048
	global_load_dwordx2 v[80:81], v[62:63], off offset:2560
	global_load_dwordx2 v[78:79], v[62:63], off offset:3072
	global_load_dwordx2 v[76:77], v[62:63], off offset:3584
	global_load_dwordx2 v[74:75], v[144:145], off
	global_load_dwordx2 v[72:73], v[144:145], off offset:512
	global_load_dwordx2 v[70:71], v[144:145], off offset:1024
	global_load_dwordx2 v[68:69], v[144:145], off offset:1536
	global_load_dwordx2 v[66:67], v[144:145], off offset:2048
	global_load_dwordx2 v[64:65], v[144:145], off offset:2560
	global_load_dwordx2 v[62:63], v[144:145], off offset:3072
	global_load_dwordx2 v[60:61], v[144:145], off offset:3584
	v_mov_b32_e32 v38, 0
	v_mov_b32_e32 v125, 0
	s_mul_i32 s8, s8, 0x880
	s_mov_b32 s9, 0
	v_lshl_add_u64 v[132:133], v[54:55], 0, s[8:9]
	s_add_i32 s8, s53, s47
	s_ashr_i32 s9, s8, 31
	s_mul_i32 s8, s8, 0x880
	s_mov_b32 s9, 0
	s_add_i32 s52, s52, s92
	s_waitcnt vmcnt(39)
	v_lshlrev_b32_e32 v144, 16, v126
	v_and_b32_e32 v126, 0xffff0000, v126
	s_waitcnt lgkmcnt(0)
	v_mul_f32_e32 v144, v14, v144
	v_mul_f32_e32 v126, v14, v126
	v_lshlrev_b32_e32 v145, 16, v127
	v_and_b32_e32 v127, 0xffff0000, v127
	s_waitcnt vmcnt(38)
	v_lshlrev_b32_e32 v150, 16, v128
	v_and_b32_e32 v128, 0xffff0000, v128
	s_waitcnt vmcnt(37)
	v_mul_f32_e32 v144, v34, v144
	v_mul_f32_e32 v126, v35, v126
	v_mul_f32_e32 v127, v14, v127
	v_mul_f32_e32 v150, v14, v150
	v_mul_f32_e32 v128, v14, v128
	v_med3_f32 v144, v144, s51, v124
	v_med3_f32 v126, v126, s51, v124
	v_mul_f32_e32 v127, v37, v127
	s_waitcnt vmcnt(36)
	v_mul_f32_e32 v150, v30, v150
	v_mul_f32_e32 v128, v31, v128
	v_cvt_pk_fp8_f32 v38, v144, v126
	v_mul_f32_e32 v145, v14, v145
	v_med3_f32 v126, v127, s51, v124
	v_med3_f32 v127, v150, s51, v124
	v_med3_f32 v128, v128, s51, v124
	v_lshlrev_b32_e32 v151, 16, v129
	v_and_b32_e32 v129, 0xffff0000, v129
	v_mul_f32_e32 v145, v36, v145
	v_cvt_pk_fp8_f32 v125, v127, v128
	v_mul_f32_e32 v151, v14, v151
	v_mul_f32_e32 v129, v14, v129
	v_med3_f32 v145, v145, s51, v124
	v_mul_f32_e32 v151, v32, v151
	v_cvt_pk_fp8_f32 v38, v145, v126 op_sel:[0,0,1]
	v_mul_f32_e32 v126, v33, v129
	v_med3_f32 v127, v151, s51, v124
	v_med3_f32 v126, v126, s51, v124
	v_cvt_pk_fp8_f32 v125, v127, v126 op_sel:[0,0,1]
	s_waitcnt vmcnt(29)
	v_lshlrev_b32_e32 v126, 16, v130
	v_and_b32_e32 v127, 0xffff0000, v130
	v_mul_f32_e32 v126, v14, v126
	v_mul_f32_e32 v127, v14, v127
	v_mul_f32_e32 v126, v26, v126
	v_mul_f32_e32 v127, v27, v127
	v_med3_f32 v126, v126, s51, v124
	v_med3_f32 v127, v127, s51, v124
	v_mov_b32_e32 v130, 0
	v_lshlrev_b32_e32 v128, 16, v131
	v_and_b32_e32 v129, 0xffff0000, v131
	v_cvt_pk_fp8_f32 v130, v126, v127
	v_mul_f32_e32 v128, v14, v128
	v_mul_f32_e32 v129, v14, v129
	v_mul_f32_e32 v128, v28, v128
	v_mul_f32_e32 v126, v29, v129
	v_med3_f32 v127, v128, s51, v124
	v_med3_f32 v126, v126, s51, v124
	v_cvt_pk_fp8_f32 v130, v127, v126 op_sel:[0,0,1]
	s_waitcnt vmcnt(28)
	v_lshlrev_b32_e32 v126, 16, v134
	v_and_b32_e32 v127, 0xffff0000, v134
	v_mul_f32_e32 v126, v14, v126
	v_mul_f32_e32 v127, v14, v127
	v_mul_f32_e32 v126, v22, v126
	v_mul_f32_e32 v127, v23, v127
	v_med3_f32 v126, v126, s51, v124
	v_med3_f32 v127, v127, s51, v124
	v_mov_b32_e32 v131, 0
	v_lshlrev_b32_e32 v128, 16, v135
	v_and_b32_e32 v129, 0xffff0000, v135
	v_cvt_pk_fp8_f32 v131, v126, v127
	v_mul_f32_e32 v128, v14, v128
	v_mul_f32_e32 v129, v14, v129
	v_mul_f32_e32 v128, v24, v128
	v_mul_f32_e32 v126, v25, v129
	v_med3_f32 v127, v128, s51, v124
	v_med3_f32 v126, v126, s51, v124
	v_cvt_pk_fp8_f32 v131, v127, v126 op_sel:[0,0,1]
	global_store_dword v[132:133], v38, off
	global_store_dword v[132:133], v125, off offset:256
	global_store_dword v[132:133], v130, off offset:512
	global_store_dword v[132:133], v131, off offset:768
	s_waitcnt vmcnt(31)
; __device__ __forceinline__ float bf_lo(unsigned u) { return __uint_as_float(u << 16); }
; __device__ __forceinline__ float bf_hi(unsigned u) { return __uint_as_float(u & 0xffff0000u); }
; __device__ __forceinline__ void p6_router(Ctx& X) {
;     ...
; #pragma unroll
;           for (int r = 0; r < 4; ++r) { const int tk = 4 * w + r, t = tb + tk; const float rstd = rs[tk];
;               unsigned* o8 = (unsigned*)(XP_U2(X) + (size_t)t * D) + lane;
; #pragma unroll
;               for (int j = 0; j < 8; ++j) { const u32x2 v = hv[r][j]; o8[64 * j] = pk_fp8x4(bf_lo(v.x) * rstd * wv[j].x, bf_hi(v.x) * rstd * wv[j].y, bf_lo(v.y) * rstd * wv[j].z, bf_hi(v.y) * rstd * wv[j].w); } } }
	v_lshlrev_b32_e32 v38, 16, v136
	v_and_b32_e32 v125, 0xffff0000, v136
	v_mul_f32_e32 v38, v14, v38
	v_mul_f32_e32 v125, v14, v125
	v_mul_f32_e32 v38, v18, v38
	v_mul_f32_e32 v125, v19, v125
	v_med3_f32 v38, v38, s51, v124
	v_med3_f32 v125, v125, s51, v124
	v_mov_b32_e32 v128, 0
	v_lshlrev_b32_e32 v126, 16, v137
	v_and_b32_e32 v127, 0xffff0000, v137
	v_cvt_pk_fp8_f32 v128, v38, v125
	v_mul_f32_e32 v126, v14, v126
	v_mul_f32_e32 v127, v14, v127
	v_mul_f32_e32 v126, v20, v126
	v_mul_f32_e32 v38, v21, v127
	v_med3_f32 v125, v126, s51, v124
	v_med3_f32 v38, v38, s51, v124
	v_cvt_pk_fp8_f32 v128, v125, v38 op_sel:[0,0,1]
	s_waitcnt vmcnt(30)
	v_lshlrev_b32_e32 v38, 16, v138
	v_and_b32_e32 v125, 0xffff0000, v138
	v_mul_f32_e32 v38, v14, v38
	v_mul_f32_e32 v125, v14, v125
	v_mul_f32_e32 v38, v10, v38
	v_mul_f32_e32 v125, v11, v125
	v_med3_f32 v38, v38, s51, v124
	v_med3_f32 v125, v125, s51, v124
	v_mov_b32_e32 v129, 0
	v_lshlrev_b32_e32 v126, 16, v139
	v_and_b32_e32 v127, 0xffff0000, v139
	v_cvt_pk_fp8_f32 v129, v38, v125
	v_mul_f32_e32 v126, v14, v126
	v_mul_f32_e32 v127, v14, v127
	v_mul_f32_e32 v126, v12, v126
	v_mul_f32_e32 v38, v13, v127
	v_med3_f32 v125, v126, s51, v124
	v_med3_f32 v38, v38, s51, v124
	v_cvt_pk_fp8_f32 v129, v125, v38 op_sel:[0,0,1]
	s_waitcnt vmcnt(29)
	v_lshlrev_b32_e32 v38, 16, v140
	v_and_b32_e32 v125, 0xffff0000, v140
	v_mul_f32_e32 v38, v14, v38
	v_mul_f32_e32 v125, v14, v125
	v_mul_f32_e32 v38, v6, v38
	v_mul_f32_e32 v125, v7, v125
	v_med3_f32 v38, v38, s51, v124
	v_med3_f32 v125, v125, s51, v124
	v_mov_b32_e32 v130, 0
	v_lshlrev_b32_e32 v126, 16, v141
	v_and_b32_e32 v127, 0xffff0000, v141
	v_cvt_pk_fp8_f32 v130, v38, v125
	v_mul_f32_e32 v126, v14, v126
	v_mul_f32_e32 v127, v14, v127
	v_mul_f32_e32 v126, v8, v126
	v_mul_f32_e32 v38, v9, v127
	v_med3_f32 v125, v126, s51, v124
	v_med3_f32 v38, v38, s51, v124
	v_cvt_pk_fp8_f32 v130, v125, v38 op_sel:[0,0,1]
	s_waitcnt vmcnt(28)
	v_lshlrev_b32_e32 v38, 16, v142
	v_and_b32_e32 v125, 0xffff0000, v142
	v_mul_f32_e32 v38, v14, v38
	v_mul_f32_e32 v125, v14, v125
	v_mul_f32_e32 v38, v2, v38
	v_mul_f32_e32 v125, v3, v125
	v_lshlrev_b32_e32 v126, 16, v143
	v_and_b32_e32 v127, 0xffff0000, v143
	v_mul_f32_e32 v126, v14, v126
	v_mul_f32_e32 v14, v14, v127
	v_med3_f32 v38, v38, s51, v124
	v_med3_f32 v125, v125, s51, v124
	v_mov_b32_e32 v127, 0
	v_cvt_pk_fp8_f32 v127, v38, v125
	v_mul_f32_e32 v126, v4, v126
	v_mul_f32_e32 v14, v5, v14
	v_med3_f32 v38, v126, s51, v124
	v_med3_f32 v14, v14, s51, v124
	v_cvt_pk_fp8_f32 v127, v38, v14 op_sel:[0,0,1]
	s_waitcnt vmcnt(27)
	v_lshlrev_b32_e32 v14, 16, v146
	v_and_b32_e32 v38, 0xffff0000, v146
	v_mul_f32_e32 v14, v15, v14
	v_mul_f32_e32 v38, v15, v38
	v_mul_f32_e32 v14, v34, v14
	v_mul_f32_e32 v38, v35, v38
	global_store_dword v[132:133], v128, off offset:1024
	global_store_dword v[132:133], v129, off offset:1280
	global_store_dword v[132:133], v130, off offset:1536
	global_store_dword v[132:133], v127, off offset:1792
	v_med3_f32 v14, v14, s51, v124
	v_med3_f32 v38, v38, s51, v124
	v_mov_b32_e32 v129, 0
	v_lshlrev_b32_e32 v125, 16, v147
	v_and_b32_e32 v128, 0xffff0000, v147
	v_cvt_pk_fp8_f32 v129, v14, v38
	v_mul_f32_e32 v125, v15, v125
	v_mul_f32_e32 v128, v15, v128
	v_mul_f32_e32 v125, v36, v125
	v_mul_f32_e32 v14, v37, v128
	v_med3_f32 v38, v125, s51, v124
	v_med3_f32 v14, v14, s51, v124
	v_cvt_pk_fp8_f32 v129, v38, v14 op_sel:[0,0,1]
	s_waitcnt vmcnt(30)
	v_lshlrev_b32_e32 v14, 16, v148
	v_and_b32_e32 v38, 0xffff0000, v148
	v_mul_f32_e32 v14, v15, v14
	v_mul_f32_e32 v38, v15, v38
	v_mul_f32_e32 v14, v30, v14
	v_mul_f32_e32 v38, v31, v38
	v_med3_f32 v14, v14, s51, v124
	v_med3_f32 v38, v38, s51, v124
	v_mov_b32_e32 v130, 0
	v_lshlrev_b32_e32 v125, 16, v149
	v_and_b32_e32 v128, 0xffff0000, v149
	v_cvt_pk_fp8_f32 v130, v14, v38
	v_mul_f32_e32 v125, v15, v125
	v_mul_f32_e32 v128, v15, v128
	v_mul_f32_e32 v125, v32, v125
	v_mul_f32_e32 v14, v33, v128
	v_med3_f32 v38, v125, s51, v124
	v_med3_f32 v14, v14, s51, v124
	v_cvt_pk_fp8_f32 v130, v38, v14 op_sel:[0,0,1]
	s_waitcnt vmcnt(29)
	v_lshlrev_b32_e32 v14, 16, v102
	v_and_b32_e32 v38, 0xffff0000, v102
	v_mul_f32_e32 v14, v15, v14
	v_mul_f32_e32 v38, v15, v38
	v_mul_f32_e32 v14, v26, v14
	v_mul_f32_e32 v38, v27, v38
	v_med3_f32 v14, v14, s51, v124
	v_med3_f32 v38, v38, s51, v124
	v_mov_b32_e32 v125, 0
	v_lshlrev_b32_e32 v102, 16, v103
	v_and_b32_e32 v103, 0xffff0000, v103
	v_cvt_pk_fp8_f32 v125, v14, v38
	v_mul_f32_e32 v102, v15, v102
	v_mul_f32_e32 v103, v15, v103
	v_mul_f32_e32 v102, v28, v102
	v_mul_f32_e32 v14, v29, v103
	v_med3_f32 v38, v102, s51, v124
	v_med3_f32 v14, v14, s51, v124
	v_cvt_pk_fp8_f32 v125, v38, v14 op_sel:[0,0,1]
	s_waitcnt vmcnt(28)
	v_lshlrev_b32_e32 v14, 16, v100
	v_and_b32_e32 v38, 0xffff0000, v100
	v_mul_f32_e32 v14, v15, v14
	v_mul_f32_e32 v38, v15, v38
	v_mul_f32_e32 v14, v22, v14
	v_mul_f32_e32 v38, v23, v38
	v_med3_f32 v14, v14, s51, v124
	v_med3_f32 v38, v38, s51, v124
	v_mov_b32_e32 v102, 0
	v_lshlrev_b32_e32 v100, 16, v101
	v_and_b32_e32 v101, 0xffff0000, v101
	v_cvt_pk_fp8_f32 v102, v14, v38
	v_mul_f32_e32 v100, v15, v100
	v_mul_f32_e32 v101, v15, v101
	v_mul_f32_e32 v100, v24, v100
	v_mul_f32_e32 v14, v25, v101
	v_med3_f32 v38, v100, s51, v124
	v_med3_f32 v14, v14, s51, v124
	v_cvt_pk_fp8_f32 v102, v38, v14 op_sel:[0,0,1]
	s_waitcnt vmcnt(27)
	v_lshlrev_b32_e32 v14, 16, v98
	v_and_b32_e32 v38, 0xffff0000, v98
	v_mul_f32_e32 v14, v15, v14
	v_mul_f32_e32 v38, v15, v38
	v_mul_f32_e32 v14, v18, v14
	v_mul_f32_e32 v38, v19, v38
	v_med3_f32 v14, v14, s51, v124
	v_med3_f32 v38, v38, s51, v124
	v_mov_b32_e32 v100, 0
	v_lshlrev_b32_e32 v98, 16, v99
	v_and_b32_e32 v99, 0xffff0000, v99
	v_cvt_pk_fp8_f32 v100, v14, v38
	v_mul_f32_e32 v98, v15, v98
	v_mul_f32_e32 v99, v15, v99
	v_mul_f32_e32 v98, v20, v98
	v_mul_f32_e32 v14, v21, v99
	v_med3_f32 v38, v98, s51, v124
	v_med3_f32 v14, v14, s51, v124
	v_cvt_pk_fp8_f32 v100, v38, v14 op_sel:[0,0,1]
	s_waitcnt vmcnt(26)
; __device__ __forceinline__ float bf_lo(unsigned u) { return __uint_as_float(u << 16); }
; __device__ __forceinline__ float bf_hi(unsigned u) { return __uint_as_float(u & 0xffff0000u); }
; __device__ __forceinline__ void p6_router(Ctx& X) {
;     ...
; #pragma unroll
;           for (int r = 0; r < 4; ++r) { const int tk = 4 * w + r, t = tb + tk; const float rstd = rs[tk];
;               unsigned* o8 = (unsigned*)(XP_U2(X) + (size_t)t * D) + lane;
; #pragma unroll
;               for (int j = 0; j < 8; ++j) { const u32x2 v = hv[r][j]; o8[64 * j] = pk_fp8x4(bf_lo(v.x) * rstd * wv[j].x, bf_hi(v.x) * rstd * wv[j].y, bf_lo(v.y) * rstd * wv[j].z, bf_hi(v.y) * rstd * wv[j].w); } } }
	v_lshlrev_b32_e32 v14, 16, v96
	v_and_b32_e32 v38, 0xffff0000, v96
	v_mul_f32_e32 v14, v15, v14
	v_mul_f32_e32 v38, v15, v38
	v_mul_f32_e32 v14, v10, v14
	v_mul_f32_e32 v38, v11, v38
	v_med3_f32 v14, v14, s51, v124
	v_med3_f32 v38, v38, s51, v124
	v_mov_b32_e32 v98, 0
	v_lshlrev_b32_e32 v96, 16, v97
	v_and_b32_e32 v97, 0xffff0000, v97
	v_cvt_pk_fp8_f32 v98, v14, v38
	v_mul_f32_e32 v96, v15, v96
	v_mul_f32_e32 v97, v15, v97
	v_mul_f32_e32 v96, v12, v96
	v_mul_f32_e32 v14, v13, v97
	v_med3_f32 v38, v96, s51, v124
	v_med3_f32 v14, v14, s51, v124
	v_cvt_pk_fp8_f32 v98, v38, v14 op_sel:[0,0,1]
	s_waitcnt vmcnt(25)
	v_lshlrev_b32_e32 v14, 16, v94
	v_and_b32_e32 v38, 0xffff0000, v94
	v_mul_f32_e32 v14, v15, v14
	v_mul_f32_e32 v38, v15, v38
	v_mul_f32_e32 v14, v6, v14
	v_mul_f32_e32 v38, v7, v38
	v_med3_f32 v14, v14, s51, v124
	v_med3_f32 v38, v38, s51, v124
	v_mov_b32_e32 v96, 0
	v_lshlrev_b32_e32 v94, 16, v95
	v_and_b32_e32 v95, 0xffff0000, v95
	v_cvt_pk_fp8_f32 v96, v14, v38
	v_mul_f32_e32 v94, v15, v94
	v_mul_f32_e32 v95, v15, v95
	v_mul_f32_e32 v94, v8, v94
	v_mul_f32_e32 v14, v9, v95
	v_med3_f32 v38, v94, s51, v124
	v_med3_f32 v14, v14, s51, v124
	v_cvt_pk_fp8_f32 v96, v38, v14 op_sel:[0,0,1]
	s_waitcnt vmcnt(24)
	v_lshlrev_b32_e32 v14, 16, v92
	v_and_b32_e32 v38, 0xffff0000, v92
	v_mul_f32_e32 v14, v15, v14
	v_mul_f32_e32 v38, v15, v38
	v_mul_f32_e32 v14, v2, v14
	v_mul_f32_e32 v38, v3, v38
	v_lshlrev_b32_e32 v92, 16, v93
	v_and_b32_e32 v93, 0xffff0000, v93
	v_mul_f32_e32 v92, v15, v92
	v_mul_f32_e32 v15, v15, v93
	v_med3_f32 v14, v14, s51, v124
	v_med3_f32 v38, v38, s51, v124
	v_mov_b32_e32 v93, 0
	v_cvt_pk_fp8_f32 v93, v14, v38
	v_mul_f32_e32 v92, v4, v92
	v_mul_f32_e32 v14, v5, v15
	s_waitcnt vmcnt(23)
	v_lshlrev_b32_e32 v38, 16, v90
	v_and_b32_e32 v90, 0xffff0000, v90
	v_med3_f32 v15, v92, s51, v124
	v_med3_f32 v14, v14, s51, v124
	v_mul_f32_e32 v38, v16, v38
	v_mul_f32_e32 v90, v16, v90
	v_lshl_add_u64 v[126:127], v[54:55], 0, s[8:9]
	v_cvt_pk_fp8_f32 v93, v15, v14 op_sel:[0,0,1]
	v_mul_f32_e32 v38, v34, v38
	v_mul_f32_e32 v90, v35, v90
	global_store_dword v[126:127], v129, off
	global_store_dword v[126:127], v130, off offset:256
	global_store_dword v[126:127], v125, off offset:512
	global_store_dword v[126:127], v102, off offset:768
	global_store_dword v[126:127], v100, off offset:1024
	global_store_dword v[126:127], v98, off offset:1280
	global_store_dword v[126:127], v96, off offset:1536
	global_store_dword v[126:127], v93, off offset:1792
	v_med3_f32 v38, v38, s51, v124
	v_med3_f32 v90, v90, s51, v124
	v_mov_b32_e32 v93, 0
	v_lshlrev_b32_e32 v92, 16, v91
	v_and_b32_e32 v91, 0xffff0000, v91
	v_cvt_pk_fp8_f32 v93, v38, v90
	v_mul_f32_e32 v92, v16, v92
	v_mul_f32_e32 v91, v16, v91
	v_mul_f32_e32 v92, v36, v92
	v_mul_f32_e32 v38, v37, v91
	v_med3_f32 v90, v92, s51, v124
	v_med3_f32 v38, v38, s51, v124
	v_cvt_pk_fp8_f32 v93, v90, v38 op_sel:[0,0,1]
	s_waitcnt vmcnt(30)
	v_lshlrev_b32_e32 v38, 16, v88
	v_and_b32_e32 v88, 0xffff0000, v88
	v_mul_f32_e32 v38, v16, v38
	v_mul_f32_e32 v88, v16, v88
	v_mul_f32_e32 v38, v30, v38
	v_mul_f32_e32 v88, v31, v88
	v_med3_f32 v38, v38, s51, v124
	v_med3_f32 v88, v88, s51, v124
	v_mov_b32_e32 v91, 0
	v_lshlrev_b32_e32 v90, 16, v89
	v_and_b32_e32 v89, 0xffff0000, v89
	v_cvt_pk_fp8_f32 v91, v38, v88
	v_mul_f32_e32 v90, v16, v90
	v_mul_f32_e32 v89, v16, v89
	v_mul_f32_e32 v90, v32, v90
	v_mul_f32_e32 v38, v33, v89
	v_med3_f32 v88, v90, s51, v124
	v_med3_f32 v38, v38, s51, v124
	v_cvt_pk_fp8_f32 v91, v88, v38 op_sel:[0,0,1]
	s_waitcnt vmcnt(29)
	v_lshlrev_b32_e32 v38, 16, v86
	v_and_b32_e32 v86, 0xffff0000, v86
	v_mul_f32_e32 v38, v16, v38
	v_mul_f32_e32 v86, v16, v86
	v_mul_f32_e32 v38, v26, v38
	v_mul_f32_e32 v86, v27, v86
	v_med3_f32 v38, v38, s51, v124
	v_med3_f32 v86, v86, s51, v124
	v_mov_b32_e32 v89, 0
	v_lshlrev_b32_e32 v88, 16, v87
	v_and_b32_e32 v87, 0xffff0000, v87
	v_cvt_pk_fp8_f32 v89, v38, v86
	v_mul_f32_e32 v88, v16, v88
	v_mul_f32_e32 v87, v16, v87
	v_mul_f32_e32 v88, v28, v88
	v_mul_f32_e32 v38, v29, v87
	v_med3_f32 v86, v88, s51, v124
	v_med3_f32 v38, v38, s51, v124
	v_cvt_pk_fp8_f32 v89, v86, v38 op_sel:[0,0,1]
	s_waitcnt vmcnt(28)
	v_lshlrev_b32_e32 v38, 16, v84
	v_and_b32_e32 v84, 0xffff0000, v84
	v_mul_f32_e32 v38, v16, v38
	v_mul_f32_e32 v84, v16, v84
	v_mul_f32_e32 v38, v22, v38
	v_mul_f32_e32 v84, v23, v84
	v_med3_f32 v38, v38, s51, v124
	v_med3_f32 v84, v84, s51, v124
	v_mov_b32_e32 v87, 0
	v_lshlrev_b32_e32 v86, 16, v85
	v_and_b32_e32 v85, 0xffff0000, v85
	v_cvt_pk_fp8_f32 v87, v38, v84
	v_mul_f32_e32 v86, v16, v86
	v_mul_f32_e32 v85, v16, v85
	v_mul_f32_e32 v86, v24, v86
	v_mul_f32_e32 v38, v25, v85
	v_med3_f32 v84, v86, s51, v124
	v_med3_f32 v38, v38, s51, v124
	v_cvt_pk_fp8_f32 v87, v84, v38 op_sel:[0,0,1]
	s_waitcnt vmcnt(27)
	v_lshlrev_b32_e32 v38, 16, v82
	v_and_b32_e32 v82, 0xffff0000, v82
	v_mul_f32_e32 v38, v16, v38
	v_mul_f32_e32 v82, v16, v82
	v_mul_f32_e32 v38, v18, v38
	v_mul_f32_e32 v82, v19, v82
	v_med3_f32 v38, v38, s51, v124
	v_med3_f32 v82, v82, s51, v124
	v_mov_b32_e32 v85, 0
	v_lshlrev_b32_e32 v84, 16, v83
	v_and_b32_e32 v83, 0xffff0000, v83
	v_cvt_pk_fp8_f32 v85, v38, v82
	v_mul_f32_e32 v84, v16, v84
	v_mul_f32_e32 v83, v16, v83
	v_mul_f32_e32 v84, v20, v84
	v_mul_f32_e32 v38, v21, v83
	v_med3_f32 v82, v84, s51, v124
	v_med3_f32 v38, v38, s51, v124
	v_cvt_pk_fp8_f32 v85, v82, v38 op_sel:[0,0,1]
	s_waitcnt vmcnt(26)
; __device__ __forceinline__ float bf_lo(unsigned u) { return __uint_as_float(u << 16); }
; __device__ __forceinline__ float bf_hi(unsigned u) { return __uint_as_float(u & 0xffff0000u); }
; __device__ __forceinline__ void p6_router(Ctx& X) {
;     ...
; #pragma unroll
;           for (int r = 0; r < 4; ++r) { const int tk = 4 * w + r, t = tb + tk; const float rstd = rs[tk];
;               unsigned* o8 = (unsigned*)(XP_U2(X) + (size_t)t * D) + lane;
; #pragma unroll
;               for (int j = 0; j < 8; ++j) { const u32x2 v = hv[r][j]; o8[64 * j] = pk_fp8x4(bf_lo(v.x) * rstd * wv[j].x, bf_hi(v.x) * rstd * wv[j].y, bf_lo(v.y) * rstd * wv[j].z, bf_hi(v.y) * rstd * wv[j].w); } } }
	v_lshlrev_b32_e32 v38, 16, v80
	v_and_b32_e32 v80, 0xffff0000, v80
	v_mul_f32_e32 v38, v16, v38
	v_mul_f32_e32 v80, v16, v80
	v_mul_f32_e32 v38, v10, v38
	v_mul_f32_e32 v80, v11, v80
	v_med3_f32 v38, v38, s51, v124
	v_med3_f32 v80, v80, s51, v124
	v_mov_b32_e32 v83, 0
	v_lshlrev_b32_e32 v82, 16, v81
	v_and_b32_e32 v81, 0xffff0000, v81
	v_cvt_pk_fp8_f32 v83, v38, v80
	v_mul_f32_e32 v82, v16, v82
	v_mul_f32_e32 v81, v16, v81
	v_mul_f32_e32 v82, v12, v82
	v_mul_f32_e32 v38, v13, v81
	v_med3_f32 v80, v82, s51, v124
	v_med3_f32 v38, v38, s51, v124
	v_cvt_pk_fp8_f32 v83, v80, v38 op_sel:[0,0,1]
	s_waitcnt vmcnt(25)
	v_lshlrev_b32_e32 v38, 16, v78
	v_and_b32_e32 v78, 0xffff0000, v78
	v_mul_f32_e32 v38, v16, v38
	v_mul_f32_e32 v78, v16, v78
	v_mul_f32_e32 v38, v6, v38
	v_mul_f32_e32 v78, v7, v78
	v_med3_f32 v38, v38, s51, v124
	v_med3_f32 v78, v78, s51, v124
	v_mov_b32_e32 v81, 0
	v_lshlrev_b32_e32 v80, 16, v79
	v_and_b32_e32 v79, 0xffff0000, v79
	v_cvt_pk_fp8_f32 v81, v38, v78
	v_mul_f32_e32 v80, v16, v80
	v_mul_f32_e32 v79, v16, v79
	v_mul_f32_e32 v80, v8, v80
	v_mul_f32_e32 v38, v9, v79
	v_med3_f32 v78, v80, s51, v124
	v_med3_f32 v38, v38, s51, v124
	v_cvt_pk_fp8_f32 v81, v78, v38 op_sel:[0,0,1]
	s_waitcnt vmcnt(24)
	v_lshlrev_b32_e32 v38, 16, v76
	v_and_b32_e32 v76, 0xffff0000, v76
	v_mul_f32_e32 v38, v16, v38
	v_mul_f32_e32 v76, v16, v76
	v_mul_f32_e32 v38, v2, v38
	v_mul_f32_e32 v76, v3, v76
	v_lshlrev_b32_e32 v78, 16, v77
	v_and_b32_e32 v77, 0xffff0000, v77
	v_mul_f32_e32 v78, v16, v78
	v_mul_f32_e32 v16, v16, v77
	v_med3_f32 v38, v38, s51, v124
	v_med3_f32 v76, v76, s51, v124
	v_mov_b32_e32 v77, 0
	v_cvt_pk_fp8_f32 v77, v38, v76
	v_mul_f32_e32 v78, v4, v78
	v_mul_f32_e32 v16, v5, v16
	v_med3_f32 v38, v78, s51, v124
	v_med3_f32 v16, v16, s51, v124
	v_cvt_pk_fp8_f32 v77, v38, v16 op_sel:[0,0,1]
	s_waitcnt vmcnt(23)
	v_lshlrev_b32_e32 v16, 16, v74
	v_mul_f32_e32 v16, v17, v16
	v_mul_f32_e32 v16, v34, v16
	v_and_b32_e32 v34, 0xffff0000, v74
	v_mul_f32_e32 v34, v17, v34
	v_mul_f32_e32 v34, v35, v34
	v_lshlrev_b32_e32 v35, 16, v75
	v_mul_f32_e32 v35, v17, v35
	v_med3_f32 v16, v16, s51, v124
	v_med3_f32 v34, v34, s51, v124
	v_mov_b32_e32 v38, 0
	v_mul_f32_e32 v35, v36, v35
	v_and_b32_e32 v36, 0xffff0000, v75
	v_cvt_pk_fp8_f32 v38, v16, v34
	v_mul_f32_e32 v36, v17, v36
	v_mul_f32_e32 v16, v37, v36
	v_med3_f32 v34, v35, s51, v124
	v_med3_f32 v16, v16, s51, v124
	v_cvt_pk_fp8_f32 v38, v34, v16 op_sel:[0,0,1]
	s_waitcnt vmcnt(22)
	v_lshlrev_b32_e32 v16, 16, v72
	v_mul_f32_e32 v16, v17, v16
	v_mul_f32_e32 v16, v30, v16
	v_and_b32_e32 v30, 0xffff0000, v72
	v_mul_f32_e32 v30, v17, v30
	v_mul_f32_e32 v30, v31, v30
	v_lshlrev_b32_e32 v31, 16, v73
	v_mul_f32_e32 v31, v17, v31
	v_med3_f32 v16, v16, s51, v124
	v_med3_f32 v30, v30, s51, v124
	v_mov_b32_e32 v34, 0
	v_mul_f32_e32 v31, v32, v31
	v_and_b32_e32 v32, 0xffff0000, v73
	v_cvt_pk_fp8_f32 v34, v16, v30
	v_mul_f32_e32 v32, v17, v32
	v_mul_f32_e32 v16, v33, v32
	v_med3_f32 v30, v31, s51, v124
	v_med3_f32 v16, v16, s51, v124
	v_cvt_pk_fp8_f32 v34, v30, v16 op_sel:[0,0,1]
	s_waitcnt vmcnt(21)
	v_lshlrev_b32_e32 v16, 16, v70
	v_mul_f32_e32 v16, v17, v16
	v_mul_f32_e32 v16, v26, v16
	v_and_b32_e32 v26, 0xffff0000, v70
	v_mul_f32_e32 v26, v17, v26
	v_mul_f32_e32 v26, v27, v26
	v_lshlrev_b32_e32 v27, 16, v71
	v_mul_f32_e32 v27, v17, v27
	v_med3_f32 v16, v16, s51, v124
	v_med3_f32 v26, v26, s51, v124
	v_mov_b32_e32 v30, 0
	v_mul_f32_e32 v27, v28, v27
	v_and_b32_e32 v28, 0xffff0000, v71
	v_cvt_pk_fp8_f32 v30, v16, v26
	v_mul_f32_e32 v28, v17, v28
	v_mul_f32_e32 v16, v29, v28
	v_med3_f32 v26, v27, s51, v124
	v_med3_f32 v16, v16, s51, v124
	v_cvt_pk_fp8_f32 v30, v26, v16 op_sel:[0,0,1]
	s_waitcnt vmcnt(20)
; __device__ __forceinline__ float bf_lo(unsigned u) { return __uint_as_float(u << 16); }
; __device__ __forceinline__ float bf_hi(unsigned u) { return __uint_as_float(u & 0xffff0000u); }
; __device__ __forceinline__ void p6_router(Ctx& X) {
;     ...
; #pragma unroll
;           for (int r = 0; r < 4; ++r) { const int tk = 4 * w + r, t = tb + tk; const float rstd = rs[tk];
;               unsigned* o8 = (unsigned*)(XP_U2(X) + (size_t)t * D) + lane;
; #pragma unroll
;               for (int j = 0; j < 8; ++j) { const u32x2 v = hv[r][j]; o8[64 * j] = pk_fp8x4(bf_lo(v.x) * rstd * wv[j].x, bf_hi(v.x) * rstd * wv[j].y, bf_lo(v.y) * rstd * wv[j].z, bf_hi(v.y) * rstd * wv[j].w); } } }
;         __syncthreads();
	v_lshlrev_b32_e32 v16, 16, v68
	v_mul_f32_e32 v16, v17, v16
	v_mul_f32_e32 v16, v22, v16
	v_and_b32_e32 v22, 0xffff0000, v68
	v_mul_f32_e32 v22, v17, v22
	v_mul_f32_e32 v22, v23, v22
	v_lshlrev_b32_e32 v23, 16, v69
	v_mul_f32_e32 v23, v17, v23
	v_med3_f32 v16, v16, s51, v124
	v_med3_f32 v22, v22, s51, v124
	v_mov_b32_e32 v26, 0
	v_mul_f32_e32 v23, v24, v23
	v_and_b32_e32 v24, 0xffff0000, v69
	v_cvt_pk_fp8_f32 v26, v16, v22
	v_mul_f32_e32 v24, v17, v24
	v_mul_f32_e32 v16, v25, v24
	v_med3_f32 v22, v23, s51, v124
	v_med3_f32 v16, v16, s51, v124
	v_cvt_pk_fp8_f32 v26, v22, v16 op_sel:[0,0,1]
	s_waitcnt vmcnt(19)
	v_lshlrev_b32_e32 v16, 16, v66
	v_mul_f32_e32 v16, v17, v16
	v_mul_f32_e32 v16, v18, v16
	v_and_b32_e32 v18, 0xffff0000, v66
	v_mul_f32_e32 v18, v17, v18
	v_mul_f32_e32 v18, v19, v18
	v_lshlrev_b32_e32 v19, 16, v67
	v_mul_f32_e32 v19, v17, v19
	v_med3_f32 v16, v16, s51, v124
	v_med3_f32 v18, v18, s51, v124
	v_mov_b32_e32 v22, 0
	v_mul_f32_e32 v19, v20, v19
	v_and_b32_e32 v20, 0xffff0000, v67
	v_cvt_pk_fp8_f32 v22, v16, v18
	v_mul_f32_e32 v20, v17, v20
	v_mul_f32_e32 v16, v21, v20
	v_med3_f32 v18, v19, s51, v124
	v_med3_f32 v16, v16, s51, v124
	v_cvt_pk_fp8_f32 v22, v18, v16 op_sel:[0,0,1]
	s_waitcnt vmcnt(18)
	v_lshlrev_b32_e32 v16, 16, v64
	v_mul_f32_e32 v16, v17, v16
	v_mul_f32_e32 v10, v10, v16
	v_and_b32_e32 v16, 0xffff0000, v64
	v_mul_f32_e32 v16, v17, v16
	v_mul_f32_e32 v11, v11, v16
	v_lshlrev_b32_e32 v16, 16, v65
	v_mul_f32_e32 v16, v17, v16
	v_med3_f32 v10, v10, s51, v124
	v_med3_f32 v11, v11, s51, v124
	v_mov_b32_e32 v18, 0
	v_mul_f32_e32 v12, v12, v16
	v_and_b32_e32 v16, 0xffff0000, v65
	v_cvt_pk_fp8_f32 v18, v10, v11
	v_mul_f32_e32 v16, v17, v16
	v_mul_f32_e32 v10, v13, v16
	v_med3_f32 v11, v12, s51, v124
	v_med3_f32 v10, v10, s51, v124
	v_cvt_pk_fp8_f32 v18, v11, v10 op_sel:[0,0,1]
	s_waitcnt vmcnt(17)
	v_lshlrev_b32_e32 v10, 16, v62
	v_mul_f32_e32 v10, v17, v10
	v_mul_f32_e32 v6, v6, v10
	v_and_b32_e32 v10, 0xffff0000, v62
	v_mul_f32_e32 v10, v17, v10
	v_mul_f32_e32 v7, v7, v10
	v_lshlrev_b32_e32 v10, 16, v63
	v_mul_f32_e32 v10, v17, v10
	v_med3_f32 v6, v6, s51, v124
	v_med3_f32 v7, v7, s51, v124
	v_mov_b32_e32 v11, 0
	v_mul_f32_e32 v8, v8, v10
	v_and_b32_e32 v10, 0xffff0000, v63
	v_cvt_pk_fp8_f32 v11, v6, v7
	v_mul_f32_e32 v10, v17, v10
	v_mul_f32_e32 v6, v9, v10
	v_med3_f32 v7, v8, s51, v124
	v_med3_f32 v6, v6, s51, v124
	v_cvt_pk_fp8_f32 v11, v7, v6 op_sel:[0,0,1]
	s_waitcnt vmcnt(16)
	v_lshlrev_b32_e32 v6, 16, v60
	v_mul_f32_e32 v6, v17, v6
	v_mul_f32_e32 v2, v2, v6
	v_and_b32_e32 v6, 0xffff0000, v60
	v_mul_f32_e32 v6, v17, v6
	s_add_i32 s8, s53, s48
	v_mul_f32_e32 v3, v3, v6
	v_lshlrev_b32_e32 v6, 16, v61
	s_ashr_i32 s9, s8, 31
	v_mul_f32_e32 v6, v17, v6
	v_med3_f32 v2, v2, s51, v124
	v_med3_f32 v3, v3, s51, v124
	v_mov_b32_e32 v7, 0
	s_mul_i32 s8, s8, 0x880
	s_mov_b32 s9, 0
	v_mul_f32_e32 v4, v4, v6
	v_and_b32_e32 v6, 0xffff0000, v61
	v_cvt_pk_fp8_f32 v7, v2, v3
	v_lshl_add_u64 v[14:15], v[54:55], 0, s[8:9]
	s_add_i32 s8, s53, s49
	v_mul_f32_e32 v6, v17, v6
	s_ashr_i32 s9, s8, 31
	v_mul_f32_e32 v2, v5, v6
	s_mul_i32 s8, s8, 0x880
	s_mov_b32 s9, 0
	v_med3_f32 v3, v4, s51, v124
	v_med3_f32 v2, v2, s51, v124
	global_store_dword v[14:15], v93, off
	global_store_dword v[14:15], v91, off offset:256
	global_store_dword v[14:15], v89, off offset:512
	global_store_dword v[14:15], v87, off offset:768
	global_store_dword v[14:15], v85, off offset:1024
	global_store_dword v[14:15], v83, off offset:1280
	global_store_dword v[14:15], v81, off offset:1536
	global_store_dword v[14:15], v77, off offset:1792
	v_lshl_add_u64 v[14:15], v[54:55], 0, s[8:9]
	v_cvt_pk_fp8_f32 v7, v3, v2 op_sel:[0,0,1]
	s_cmpk_lt_i32 s52, 0x100
	global_store_dword v[14:15], v38, off
	global_store_dword v[14:15], v34, off offset:256
	global_store_dword v[14:15], v30, off offset:512
	global_store_dword v[14:15], v26, off offset:768
	global_store_dword v[14:15], v22, off offset:1024
	global_store_dword v[14:15], v18, off offset:1280
	global_store_dword v[14:15], v11, off offset:1536
	global_store_dword v[14:15], v7, off offset:1792
	s_barrier
	s_cbranch_scc0 .LBB0_834

; #define LAS __attribute__((address_space(3)))
; #define PG8_WAIT_V(n) asm volatile("s_waitcnt vmcnt(" #n ")" ::: "memory")
; #define PG8_BAR __builtin_amdgcn_s_barrier()
; template <class Epi, class Sched, bool GATHER, bool FP8>
; __device__ __forceinline__ void gemm_phase(LAS uchar* lds, const int K, const int LDA, const int LDB, const size_t kstepA, const size_t kstepB, const Sched& S, const Epi& E) {
;     ...
;     const char* cA = cur.pa; const char* cB = cur.pb;
;     if constexpr (GATHER) S.gather(cur, voA, (const LAS int*)nullptr);
;     PG8_STAGE(PG8_SB(0, 0), cB, voffB); PG8_STAGE(PG8_SB(0, 1), cB + hstep, voffB); PG8_STAGE(PG8_SA(0, 0), cA, voA[0]); PG8_STAGE(PG8_SA(0, 1), cA, voA[1]);
;     if (wr == 1) PG8_BAR;
;     PG8_WAIT_V(2); PG8_BAR;
;     PG8_STAGE(PG8_SB(1, 0), cB + kstepB, voffB); PG8_STAGE(PG8_SA(1, 0), cA + kstepA, voA[0]); PG8_STAGE(PG8_SB(1, 1), cB + hstep + kstepB, voffB);
;     __device__ __forceinline__ bool next(int i, pg8::Unit& u) const {
;         const int NB = __builtin_amdgcn_readfirstlane(tab[0]); const int L = i * G + c; if (L >= NB * nN) return false;
;         const int b = L / nN, pn = L - b * nN, e = __builtin_amdgcn_readfirstlane(tab[64 + b]);
;         u.pa = A; u.pb = B + (size_t)e * bexp + (size_t)pn * 256 * 128; u.row0 = b * 256; u.col0 = pn * 256; u.aux = e; u.blk = b; return true;
;     }
;     __device__ __forceinline__ void prefetch(const pg8::Unit& u, LAS uchar* buf, int wid, int lane) const {
;         { const int e = u.aux, lb = (u.blk - __builtin_amdgcn_readfirstlane(tab[8 + e])) * 256, w4 = wid & 3;
;             __builtin_amdgcn_global_load_lds((const unsigned*)(list + e * T + lb + 64 * w4 + lane), (LAS unsigned*)(buf + w4 * 256), 4, 0, 0); }
;     }
;     __device__ __forceinline__ void gather(const pg8::Unit& u, unsigned (&vo)[2][2], const LAS int* idx) const {
;         const int e = u.aux, lb = (u.blk - __builtin_amdgcn_readfirstlane(tab[8 + e])) * 256, cnt = __builtin_amdgcn_readfirstlane(tab[256 + u.blk]);
; #pragma unroll
;         for (int i = 0; i < 2; ++i) { int R, C; pg8::stage_rc((int)threadIdx.x * 16 + i * 8192, R, C);
; #pragma unroll
;             for (int h = 0; h < 2; ++h) { const int r = h * 128 + R; const int raw = idx ? idx[r] : list[e * T + lb + r]; const int tok = (r < cnt) ? raw : 0; vo[h][i] = ((unsigned)tok * (unsigned)K + (unsigned)C) * 2u; } }
;     }
.LBB0_917:
	s_or_b64 exec, exec, s[8:9]
	s_add_i32 s12, 0, 0x22000
	s_waitcnt vmcnt(4)
	v_mov_b32_e32 v2, s12
	s_waitcnt lgkmcnt(0)
	s_barrier
	ds_read_b32 v2, v2
	v_readfirstlane_b32 s20, v0
	s_waitcnt lgkmcnt(0)
	v_readfirstlane_b32 s2, v2
	s_lshl_b32 s2, s2, 4
	s_and_b32 s99, s87, 3
	s_lshl_b32 s98, s99, 6
	s_lshr_b32 s99, s87, 6
	s_lshl_b32 s99, s99, 4
	s_or_b32 s98, s98, s99
	s_bfe_u32 s99, s87, 0x10002
	s_lshl_b32 s99, s99, 3
	s_or_b32 s98, s98, s99
	s_bfe_u32 s99, s87, 0x30003
	s_or_b32 s98, s98, s99
	s_cmpk_eq_i32 s92, 0x100
	s_cselect_b32 s98, s98, s87
	s_cmp_ge_i32 s98, s2
	s_cbranch_scc1 .LBB0_937
	s_add_u32 s8, s90, 0x6000000
	s_addc_u32 s9, s91, 0
	s_add_u32 s25, s90, 0x30000000
	s_addc_u32 s33, s91, 0
	s_add_u32 s10, s90, 0x2f00000
	s_addc_u32 s11, s91, 0
	s_ashr_i32 s2, s98, 31
	s_lshr_b32 s2, s2, 28
	s_add_i32 s2, s98, s2
	s_ashr_i32 s18, s2, 4
	s_lshl_b32 s3, s18, 2
	s_add_i32 s3, s12, s3
	v_mov_b32_e32 v2, s3
	ds_read2st64_b32 v[2:3], v2 offset0:1 offset1:4
	s_lshr_b32 s21, s20, 6
	s_and_b32 s2, s2, -16
	s_lshr_b32 s22, s20, 8
	s_lshl_b32 s52, s21, 10
	s_waitcnt lgkmcnt(0)
	v_readfirstlane_b32 s42, v2
	s_ashr_i32 s43, s42, 31
	s_sub_i32 s2, s98, s2
	s_lshl_b64 s[14:15], s[42:43], 23
	s_add_u32 s13, s25, s14
	s_addc_u32 s16, s33, s15
	s_ashr_i32 s3, s2, 31
	s_lshl_b64 s[14:15], s[2:3], 15
	s_add_u32 s44, s13, s14
	s_addc_u32 s45, s16, s15
	s_lshl_b32 s3, s42, 2
	s_add_i32 s3, s12, s3
	v_mov_b32_e32 v2, s3
	ds_read_b32 v2, v2 offset:32
	v_lshrrev_b32_e32 v13, 3, v0
	v_bfe_u32 v12, v0, 2, 4
	v_or_b32_e32 v4, 64, v13
	s_movk_i32 s3, 0x70
	v_and_or_b32 v195, v4, s3, v12
	s_waitcnt lgkmcnt(0)
	v_readfirstlane_b32 s3, v2
	s_sub_i32 s3, s18, s3
	s_lshl_b32 s3, s3, 8
	s_lshl_b32 s12, s42, 13
	s_add_i32 s3, s3, s12
	v_and_or_b32 v208, v13, 48, v12
	v_or_b32_e32 v4, s3, v208
	v_or_b32_e32 v209, 0x80, v208
	v_or_b32_e32 v210, 0x80, v195
	v_ashrrev_i32_e32 v5, 31, v4
	v_or_b32_e32 v6, s3, v209
	v_or_b32_e32 v8, s3, v195
	v_or_b32_e32 v10, s3, v210
	v_lshl_add_u64 v[4:5], v[4:5], 2, s[10:11]
	v_ashrrev_i32_e32 v7, 31, v6
	v_ashrrev_i32_e32 v9, 31, v8
	v_ashrrev_i32_e32 v11, 31, v10
	v_lshl_add_u64 v[6:7], v[6:7], 2, s[10:11]
	v_lshl_add_u64 v[8:9], v[8:9], 2, s[10:11]
	v_lshl_add_u64 v[10:11], v[10:11], 2, s[10:11]
	global_load_dword v14, v[4:5], off
	global_load_dword v15, v[6:7], off
	global_load_dword v16, v[8:9], off
	global_load_dword v17, v[10:11], off
	v_lshlrev_b32_e32 v4, 4, v0
	v_and_b32_e32 v5, 32, v0
	v_bitop3_b32 v4, v4, v5, 48 bitop3:0x6c
	v_and_or_b32 v5, v13, 32, v12
	v_and_b32_e32 v2, 48, v0
	s_movk_i32 s14, 0x46
	v_and_or_b32 v211, v0, 64, v4
	v_lshlrev_b32_e32 v4, 1, v5
	s_movk_i32 s3, 0xc6
	v_lshlrev_b32_e32 v5, 1, v195
	v_and_or_b32 v4, v4, s14, v2
	s_add_i32 s53, s52, 0
	v_and_b32_e32 v6, 0x80, v0
	v_mov_b32_e32 v197, 0
	v_and_or_b32 v5, v5, s3, v2
	v_lshlrev_b32_e32 v4, 7, v4
	s_add_i32 s54, s53, 0x10000
	v_mov_b32_e32 v199, v197
	v_lshlrev_b32_e32 v5, 7, v5
	v_or3_b32 v198, v4, v6, v211
	s_add_i32 s55, s53, 0x12000
	s_mov_b32 m0, s54
	s_mov_b64 s[12:13], 0x400
	v_or3_b32 v200, v5, v6, v211
	v_readfirstlane_b32 s3, v3
	v_lshl_add_u64 v[4:5], s[44:45], 0, v[198:199]
	s_add_i32 s56, s53, 0x14000
	global_load_lds_dwordx4 v198, s[44:45]
	s_mov_b32 m0, s55
	v_mov_b32_e32 v201, v197
	v_lshl_add_u64 v[4:5], v[4:5], 0, s[12:13]
	global_load_lds_dwordx4 v200, s[44:45]
	s_mov_b32 m0, s56
	v_cmp_gt_i32_e32 vcc, s3, v208
	v_lshl_add_u64 v[6:7], s[44:45], 0, v[200:201]
	s_add_i32 s57, s53, 0x16000
	global_load_lds_dwordx4 v[4:5], off
	v_lshl_add_u64 v[6:7], v[6:7], 0, s[12:13]
	s_mov_b32 m0, s57
	s_add_i32 s58, s53, 0x2000
	global_load_lds_dwordx4 v[6:7], off
	s_mov_b32 m0, s53
	s_add_i32 s59, s53, 0x4000
	s_add_i32 s60, s53, 0x6000
	s_load_dwordx2 s[14:15], s[0:1], 0x78
	s_cmp_eq_u32 s22, 1
	s_mov_b32 s46, 0
	s_cselect_b64 s[16:17], -1, 0
	s_cmp_lg_u32 s22, 1
	v_mov_b32_e32 v203, v197
	s_waitcnt vmcnt(0)
	v_mul_u32_u24_e32 v3, 0x880, v14
	v_mul_u32_u24_e32 v4, 0x880, v15
	v_cndmask_b32_e32 v3, 0, v3, vcc
	v_cmp_gt_i32_e32 vcc, s3, v209
	v_mul_u32_u24_e32 v5, 0x880, v16
	v_or_b32_e32 v196, v3, v211
	v_cndmask_b32_e32 v4, 0, v4, vcc
	v_cmp_gt_i32_e32 vcc, s3, v195
	v_mul_u32_u24_e32 v6, 0x880, v17
	global_load_lds_dwordx4 v196, s[8:9]
	v_cndmask_b32_e32 v5, 0, v5, vcc
	v_cmp_gt_i32_e32 vcc, s3, v210
	v_or_b32_e32 v202, v5, v211
	s_mov_b32 m0, s58
	v_cndmask_b32_e32 v6, 0, v6, vcc
	v_or_b32_e32 v3, v4, v211
	global_load_lds_dwordx4 v202, s[8:9]
	s_mov_b32 m0, s59
	v_or_b32_e32 v204, v6, v211
	global_load_lds_dwordx4 v3, s[8:9]
	s_mov_b32 m0, s60
	s_nop 0
	global_load_lds_dwordx4 v204, s[8:9]
	s_cbranch_scc1 .LBB0_920
	s_barrier

; #define LAS __attribute__((address_space(3)))
; #define PG8_STAGE(bufoff, gbase, voff) do { _Pragma("unroll") for (int _i = 0; _i < 2; ++_i) \
;         __builtin_amdgcn_global_load_lds((const unsigned*)((const char*)(gbase) + (voff)[_i]), (LAS unsigned*)(lds + (bufoff) + ldsw + _i * 8192), 16, 0, 0); } while (0)
; #define PG8_LDA(dst, b, h) do { _Pragma("unroll") for (int m = 0; m < 4; ++m) _Pragma("unroll") for (int k = 0; k < 2; ++k) dst[m][k] = *(const LAS bf16x8*)(lds + PG8_SA(b, h) + aoff + m * 2048 + k * 1024); } while (0)
; #define PG8_LDB(dst, b, h) do { _Pragma("unroll") for (int n = 0; n < 2; ++n) _Pragma("unroll") for (int k = 0; k < 2; ++k) dst[n][k] = *(const LAS bf16x8*)(lds + PG8_SB(b, h) + boff + n * 2048 + k * 1024); } while (0)
; template <class Epi, class Sched, bool GATHER, bool FP8>
; __device__ __forceinline__ void gemm_phase(LAS uchar* lds, const int K, const int LDA, const int LDB, const size_t kstepA, const size_t kstepB, const Sched& S, const Epi& E) {
;     ...
;             const bool last = (t == nt - 2);
;             const char* a1 = cA + (size_t)(t + 1) * kstepA;
;             const char* a2 = last ? nA : cA + (size_t)(t + 2) * kstepA; const char* b2 = last ? nB : cB + (size_t)(t + 2) * kstepB;
;             const char* a3 = a2 + kstepA; const char* b3 = b2 + kstepB;
;             int fresh; { const int fv = (t == 0 && ui > 0) ? 1 : 0; asm volatile("s_nop 0\n\tv_readfirstlane_b32 %0, %1" : "=s"(fresh) : "v"(fv)); }
;             PG8_LDB(B0, 0, 0); PG8_LDB(B1, 0, 1); PG8_SCHED; PG8_LDA(At, 0, 0); PG8_STAGE(PG8_SA(1, 1), a1, voA[1]);
;             if constexpr (GATHER) { if (last && has_next) S.gather(nxt, voA, (const LAS int*)(lds + LDS_IDX + ((ui + 1) & 1) * 1024)); }
;     __device__ __forceinline__ void gather(const pg8::Unit& u, unsigned (&vo)[2][2], const LAS int* idx) const {
;         const int e = u.aux, lb = (u.blk - __builtin_amdgcn_readfirstlane(tab[8 + e])) * 256, cnt = __builtin_amdgcn_readfirstlane(tab[256 + u.blk]);
; #pragma unroll
;         for (int i = 0; i < 2; ++i) { int R, C; pg8::stage_rc((int)threadIdx.x * 16 + i * 8192, R, C);
; #pragma unroll
;             for (int h = 0; h < 2; ++h) { const int r = h * 128 + R; const int raw = idx ? idx[r] : list[e * T + lb + r]; const int tok = (r < cnt) ? raw : 0; vo[h][i] = ((unsigned)tok * (unsigned)K + (unsigned)C) * 2u; } }
;     }
.LBB0_929:
	s_cmpk_eq_i32 s44, 0x700
	s_cselect_b64 s[46:47], -1, 0
	s_cmp_eq_u32 s44, 0
	s_cselect_b64 s[48:49], -1, 0
	s_and_b64 s[48:49], s[42:43], s[48:49]
	v_cndmask_b32_e64 v2, 0, 1, s[48:49]
	s_nop 0
	v_readfirstlane_b32 s78, v2
	ds_read_b128 v[18:21], v215
	ds_read_b128 v[22:25], v215 offset:1024
	ds_read_b128 v[26:29], v215 offset:2048
	ds_read_b128 v[30:33], v215 offset:3072
	ds_read_b128 v[2:5], v216
	ds_read_b128 v[6:9], v216 offset:1024
	ds_read_b128 v[10:13], v216 offset:2048
	ds_read_b128 v[14:17], v216 offset:3072
	s_add_u32 s48, s38, s44
	s_addc_u32 s49, s39, s45
	v_lshl_add_u64 v[222:223], s[48:49], 0, v[196:197]
	v_lshl_add_u64 v[222:223], v[222:223], 0, s[22:23]
	s_add_i32 m0, s53, 0xc000
	v_mov_b32_e32 v205, v197
	ds_read_b128 v[58:61], v217
	ds_read_b128 v[62:65], v217 offset:1024
	ds_read_b128 v[50:53], v217 offset:2048
	ds_read_b128 v[54:57], v217 offset:3072
	ds_read_b128 v[42:45], v217 offset:4096
	ds_read_b128 v[46:49], v217 offset:5120
	ds_read_b128 v[34:37], v217 offset:6144
	ds_read_b128 v[38:41], v217 offset:7168
	global_load_lds_dwordx4 v[222:223], off
	v_lshl_add_u64 v[222:223], s[48:49], 0, v[204:205]
	v_lshl_add_u64 v[222:223], v[222:223], 0, s[22:23]
	s_add_i32 m0, s53, 0xe000
	s_and_b64 s[48:49], s[40:41], s[46:47]
	global_load_lds_dwordx4 v[222:223], off
	s_andn2_b64 vcc, exec, s[48:49]
	s_cbranch_vccnz .LBB0_928
	v_mov_b32_e32 v196, s74
	ds_read2st64_b32 v[202:203], v220 offset1:2
	ds_read_b32 v196, v196 offset:1024
	ds_read2st64_b32 v[204:205], v221 offset1:2
	s_waitcnt lgkmcnt(0)
	v_mul_u32_u24_e32 v202, 0x880, v202
	v_readfirstlane_b32 s48, v196
	s_nop 1
	v_cmp_gt_i32_e32 vcc, s48, v208
	s_nop 1
	v_cndmask_b32_e32 v196, 0, v202, vcc
	v_or_b32_e32 v206, v196, v211
	v_mul_u32_u24_e32 v196, 0x880, v203
	v_cmp_gt_i32_e32 vcc, s48, v209
	v_mul_u32_u24_e32 v202, 0x880, v204
	v_mul_u32_u24_e32 v203, 0x880, v205
	v_cndmask_b32_e32 v196, 0, v196, vcc
	v_cmp_gt_i32_e32 vcc, s48, v195
	v_or_b32_e32 v196, v196, v211
	v_mov_b32_e32 v205, v197
	v_cndmask_b32_e32 v202, 0, v202, vcc
	v_cmp_gt_i32_e32 vcc, s48, v210
	v_or_b32_e32 v202, v202, v211
	s_nop 0
	v_cndmask_b32_e32 v203, 0, v203, vcc
	v_or_b32_e32 v204, v203, v211
	s_branch .LBB0_928
